# DSA unit header: first 8 K-tile loads hoisted above the q wait + qs compute (on top of v38)
# speedup vs baseline: 1.0122x; 1.0031x over previous
.LBB0_706:
	s_or_b64 exec, exec, s[0:1]
	s_lshl_b32 s2, s16, 2
	s_andn2_b32 s2, s2, 31
	s_and_b32 s0, s16, 7
	s_and_b32 s1, s13, 1
	s_xor_b32 s6, s2, 0x3e0
	s_cmp_eq_u32 s1, 0
	s_cselect_b32 s1, s2, s6
	s_sub_i32 s6, 0x1fe0, s1
	s_lshl_b32 s25, s0, 13
	s_add_i32 s8, s6, s25
	s_lshl_b32 s2, s0, 20
	s_ashr_i32 s9, s8, 31
	s_ashr_i32 s7, s6, 5
	v_readlane_b32 s0, v254, 49
	s_add_u32 s0, s0, s2
	v_readlane_b32 s1, v254, 50
	s_addc_u32 s1, s1, 0
	s_lshl_b64 s[10:11], s[8:9], 5
	v_lshl_add_u64 v[2:3], v[146:147], 0, s[10:11]
	s_waitcnt lgkmcnt(0)
	s_barrier
	global_load_dwordx4 v[66:69], v[2:3], off
	global_load_dwordx4 v[70:73], v[2:3], off offset:16
	s_lshl_b64 s[8:9], s[8:9], 10
	v_lshl_add_u64 v[62:63], v[144:145], 0, s[8:9]
	global_load_dwordx4 v[2:5], v[62:63], off
	global_load_dwordx4 v[6:9], v[62:63], off offset:128
	global_load_dwordx4 v[10:13], v[62:63], off offset:256
	global_load_dwordx4 v[14:17], v[62:63], off offset:384
	global_load_dwordx4 v[18:21], v[62:63], off offset:512
	global_load_dwordx4 v[22:25], v[62:63], off offset:640
	global_load_dwordx4 v[26:29], v[62:63], off offset:768
	global_load_dwordx4 v[30:33], v[62:63], off offset:896
	global_load_dwordx4 v[34:37], v[62:63], off offset:64
	global_load_dwordx4 v[38:41], v[62:63], off offset:192
	global_load_dwordx4 v[42:45], v[62:63], off offset:320
	global_load_dwordx4 v[46:49], v[62:63], off offset:448
	global_load_dwordx4 v[50:53], v[62:63], off offset:576
	global_load_dwordx4 v[54:57], v[62:63], off offset:704
	global_load_dwordx4 v[58:61], v[62:63], off offset:832
	s_nop 0
	global_load_dwordx4 v[62:65], v[62:63], off offset:960
	v_lshl_add_u64 v[184:185], s[0:1], 0, v[152:153]
	v_lshl_add_u64 v[184:185], v[184:185], 0, v[154:155]
	s_mov_b64 s[10:11], 0x800
	v_lshl_add_u64 v[186:187], v[184:185], 0, s[10:11]
	global_load_dwordx4 v[134:137], v[184:185], off
	global_load_dwordx4 v[130:133], v[184:185], off offset:1024
	s_mov_b64 s[10:11], 0x1000
	v_lshl_add_u64 v[188:189], v[184:185], 0, s[10:11]
	global_load_dwordx4 v[126:129], v[186:187], off
	global_load_dwordx4 v[122:125], v[186:187], off offset:1024
	s_mov_b64 s[10:11], 0x1800
	v_lshl_add_u64 v[184:185], v[184:185], 0, s[10:11]
	global_load_dwordx4 v[110:113], v[188:189], off
	global_load_dwordx4 v[106:109], v[188:189], off offset:1024
	global_load_dwordx4 v[94:97], v[184:185], off
	global_load_dwordx4 v[90:93], v[184:185], off offset:1024
	s_add_i32 s7, s7, 1
	s_ashr_i32 s9, s6, 4
	s_lshl_b32 s8, s7, 1
	v_lshl_add_u64 v[172:173], s[0:1], 0, v[154:155]
	s_waitcnt vmcnt(23)
	v_and_b32_e32 v83, 0xffff0000, v3
	v_lshlrev_b32_e32 v82, 16, v3
	s_waitcnt vmcnt(22)
	v_and_b32_e32 v85, 0xffff0000, v7
	v_mul_f32_e32 v156, 0.5, v66
	v_mul_f32_e32 v158, 0.5, v67
	v_and_b32_e32 v67, 0xffff0000, v2
	v_lshlrev_b32_e32 v66, 16, v2
	v_mul_f32_e32 v160, 0.5, v68
	v_mul_f32_e32 v162, 0.5, v69
	v_and_b32_e32 v69, 0xffff0000, v6
	v_lshlrev_b32_e32 v68, 16, v6
	v_lshlrev_b32_e32 v84, 16, v7
	v_pk_fma_f32 v[66:67], v[156:157], v[66:67], 0 op_sel_hi:[0,1,0]
	v_pk_fma_f32 v[82:83], v[156:157], v[82:83], 0 op_sel_hi:[0,1,0]
	v_mul_f32_e32 v164, 0.5, v70
	v_mul_f32_e32 v166, 0.5, v71
	s_waitcnt vmcnt(21)
	v_and_b32_e32 v71, 0xffff0000, v10
	v_lshlrev_b32_e32 v70, 16, v10
	v_and_b32_e32 v87, 0xffff0000, v11
	v_lshlrev_b32_e32 v86, 16, v11
	v_pk_fma_f32 v[66:67], v[158:159], v[68:69], v[66:67] op_sel_hi:[0,1,1]
	v_pk_fma_f32 v[68:69], v[158:159], v[84:85], v[82:83] op_sel_hi:[0,1,1]
	v_mul_f32_e32 v168, 0.5, v72
	v_mul_f32_e32 v170, 0.5, v73
	s_waitcnt vmcnt(20)
	v_and_b32_e32 v73, 0xffff0000, v14
	v_lshlrev_b32_e32 v72, 16, v14
	v_and_b32_e32 v89, 0xffff0000, v15
	v_lshlrev_b32_e32 v88, 16, v15
	v_pk_fma_f32 v[66:67], v[160:161], v[70:71], v[66:67] op_sel_hi:[0,1,1]
	v_pk_fma_f32 v[68:69], v[160:161], v[86:87], v[68:69] op_sel_hi:[0,1,1]
	s_waitcnt vmcnt(19)
	v_and_b32_e32 v75, 0xffff0000, v18
	v_lshlrev_b32_e32 v74, 16, v18
	v_and_b32_e32 v177, 0xffff0000, v19
	v_lshlrev_b32_e32 v176, 16, v19
	v_pk_fma_f32 v[66:67], v[162:163], v[72:73], v[66:67] op_sel_hi:[0,1,1]
	v_pk_fma_f32 v[68:69], v[162:163], v[88:89], v[68:69] op_sel_hi:[0,1,1]
	s_waitcnt vmcnt(18)
	v_and_b32_e32 v77, 0xffff0000, v22
	v_lshlrev_b32_e32 v76, 16, v22
	v_and_b32_e32 v179, 0xffff0000, v23
	v_lshlrev_b32_e32 v178, 16, v23
	v_pk_fma_f32 v[66:67], v[164:165], v[74:75], v[66:67] op_sel_hi:[0,1,1]
	v_pk_fma_f32 v[68:69], v[164:165], v[176:177], v[68:69] op_sel_hi:[0,1,1]
	s_waitcnt vmcnt(17)
	v_and_b32_e32 v79, 0xffff0000, v26
	v_lshlrev_b32_e32 v78, 16, v26
	v_and_b32_e32 v181, 0xffff0000, v27
	v_lshlrev_b32_e32 v180, 16, v27
	v_pk_fma_f32 v[66:67], v[166:167], v[76:77], v[66:67] op_sel_hi:[0,1,1]
	v_pk_fma_f32 v[68:69], v[166:167], v[178:179], v[68:69] op_sel_hi:[0,1,1]
	s_waitcnt vmcnt(16)
	v_and_b32_e32 v81, 0xffff0000, v30
	v_lshlrev_b32_e32 v80, 16, v30
	v_and_b32_e32 v183, 0xffff0000, v31
	v_lshlrev_b32_e32 v182, 16, v31
	v_pk_fma_f32 v[66:67], v[168:169], v[78:79], v[66:67] op_sel_hi:[0,1,1]
	v_pk_fma_f32 v[68:69], v[168:169], v[180:181], v[68:69] op_sel_hi:[0,1,1]
	v_and_b32_e32 v99, 0xffff0000, v4
	v_lshlrev_b32_e32 v98, 16, v4
	v_pk_fma_f32 v[66:67], v[170:171], v[80:81], v[66:67] op_sel_hi:[0,1,1]
	v_pk_fma_f32 v[68:69], v[170:171], v[182:183], v[68:69] op_sel_hi:[0,1,1]
	v_cvt_pk_bf16_f32 v66, v66, v67
	v_cvt_pk_bf16_f32 v67, v68, v69
	v_pk_fma_f32 v[68:69], v[156:157], v[98:99], 0 op_sel_hi:[0,1,0]
	v_and_b32_e32 v71, 0xffff0000, v8
	v_lshlrev_b32_e32 v70, 16, v8
	v_pk_fma_f32 v[68:69], v[158:159], v[70:71], v[68:69] op_sel_hi:[0,1,1]
	v_and_b32_e32 v71, 0xffff0000, v12
	v_lshlrev_b32_e32 v70, 16, v12
	v_pk_fma_f32 v[68:69], v[160:161], v[70:71], v[68:69] op_sel_hi:[0,1,1]
	v_and_b32_e32 v71, 0xffff0000, v16
	v_lshlrev_b32_e32 v70, 16, v16
	v_pk_fma_f32 v[68:69], v[162:163], v[70:71], v[68:69] op_sel_hi:[0,1,1]
	v_and_b32_e32 v71, 0xffff0000, v20
	v_lshlrev_b32_e32 v70, 16, v20
	v_pk_fma_f32 v[68:69], v[164:165], v[70:71], v[68:69] op_sel_hi:[0,1,1]
	v_and_b32_e32 v71, 0xffff0000, v24
	v_lshlrev_b32_e32 v70, 16, v24
	v_pk_fma_f32 v[68:69], v[166:167], v[70:71], v[68:69] op_sel_hi:[0,1,1]
	v_and_b32_e32 v71, 0xffff0000, v28
	v_lshlrev_b32_e32 v70, 16, v28
	v_pk_fma_f32 v[68:69], v[168:169], v[70:71], v[68:69] op_sel_hi:[0,1,1]
	v_and_b32_e32 v71, 0xffff0000, v32
	v_lshlrev_b32_e32 v70, 16, v32
	v_pk_fma_f32 v[68:69], v[170:171], v[70:71], v[68:69] op_sel_hi:[0,1,1]
	v_and_b32_e32 v71, 0xffff0000, v5
	v_lshlrev_b32_e32 v70, 16, v5
	v_pk_fma_f32 v[70:71], v[156:157], v[70:71], 0 op_sel_hi:[0,1,0]
	v_and_b32_e32 v73, 0xffff0000, v9
	v_lshlrev_b32_e32 v72, 16, v9
	v_pk_fma_f32 v[70:71], v[158:159], v[72:73], v[70:71] op_sel_hi:[0,1,1]
	v_and_b32_e32 v73, 0xffff0000, v13
	v_lshlrev_b32_e32 v72, 16, v13
	v_pk_fma_f32 v[70:71], v[160:161], v[72:73], v[70:71] op_sel_hi:[0,1,1]
	v_and_b32_e32 v73, 0xffff0000, v17
	v_lshlrev_b32_e32 v72, 16, v17
	v_pk_fma_f32 v[70:71], v[162:163], v[72:73], v[70:71] op_sel_hi:[0,1,1]
	v_and_b32_e32 v73, 0xffff0000, v21
	v_lshlrev_b32_e32 v72, 16, v21
	v_pk_fma_f32 v[70:71], v[164:165], v[72:73], v[70:71] op_sel_hi:[0,1,1]
	v_and_b32_e32 v73, 0xffff0000, v25
	v_lshlrev_b32_e32 v72, 16, v25
	v_pk_fma_f32 v[70:71], v[166:167], v[72:73], v[70:71] op_sel_hi:[0,1,1]
	v_and_b32_e32 v73, 0xffff0000, v29
	v_lshlrev_b32_e32 v72, 16, v29
	v_pk_fma_f32 v[70:71], v[168:169], v[72:73], v[70:71] op_sel_hi:[0,1,1]
	v_and_b32_e32 v73, 0xffff0000, v33
	v_lshlrev_b32_e32 v72, 16, v33
	v_pk_fma_f32 v[70:71], v[170:171], v[72:73], v[70:71] op_sel_hi:[0,1,1]
	v_cvt_pk_bf16_f32 v68, v68, v69
	v_cvt_pk_bf16_f32 v69, v70, v71
	s_waitcnt vmcnt(15)
	v_and_b32_e32 v71, 0xffff0000, v34
	v_lshlrev_b32_e32 v70, 16, v34
	v_pk_fma_f32 v[70:71], v[156:157], v[70:71], 0 op_sel_hi:[0,1,0]
	s_waitcnt vmcnt(14)
	v_and_b32_e32 v73, 0xffff0000, v38
	v_lshlrev_b32_e32 v72, 16, v38
	v_pk_fma_f32 v[70:71], v[158:159], v[72:73], v[70:71] op_sel_hi:[0,1,1]
	s_waitcnt vmcnt(13)
	v_and_b32_e32 v73, 0xffff0000, v42
	v_lshlrev_b32_e32 v72, 16, v42
	v_pk_fma_f32 v[70:71], v[160:161], v[72:73], v[70:71] op_sel_hi:[0,1,1]
	s_waitcnt vmcnt(12)
	v_and_b32_e32 v73, 0xffff0000, v46
	v_lshlrev_b32_e32 v72, 16, v46
	v_pk_fma_f32 v[70:71], v[162:163], v[72:73], v[70:71] op_sel_hi:[0,1,1]
	s_waitcnt vmcnt(11)
	v_and_b32_e32 v73, 0xffff0000, v50
	v_lshlrev_b32_e32 v72, 16, v50
	v_pk_fma_f32 v[70:71], v[164:165], v[72:73], v[70:71] op_sel_hi:[0,1,1]
	s_waitcnt vmcnt(10)
	v_and_b32_e32 v73, 0xffff0000, v54
	v_lshlrev_b32_e32 v72, 16, v54
	v_pk_fma_f32 v[70:71], v[166:167], v[72:73], v[70:71] op_sel_hi:[0,1,1]
	s_waitcnt vmcnt(9)
	v_and_b32_e32 v73, 0xffff0000, v58
	v_lshlrev_b32_e32 v72, 16, v58
	v_pk_fma_f32 v[70:71], v[168:169], v[72:73], v[70:71] op_sel_hi:[0,1,1]
	s_waitcnt vmcnt(8)
	v_and_b32_e32 v73, 0xffff0000, v62
	v_lshlrev_b32_e32 v72, 16, v62
	v_pk_fma_f32 v[70:71], v[170:171], v[72:73], v[70:71] op_sel_hi:[0,1,1]
	v_and_b32_e32 v73, 0xffff0000, v35
	v_lshlrev_b32_e32 v72, 16, v35
	v_pk_fma_f32 v[72:73], v[156:157], v[72:73], 0 op_sel_hi:[0,1,0]
	v_and_b32_e32 v75, 0xffff0000, v39
	v_lshlrev_b32_e32 v74, 16, v39
	v_pk_fma_f32 v[72:73], v[158:159], v[74:75], v[72:73] op_sel_hi:[0,1,1]
	v_and_b32_e32 v75, 0xffff0000, v43
	v_lshlrev_b32_e32 v74, 16, v43
	v_pk_fma_f32 v[72:73], v[160:161], v[74:75], v[72:73] op_sel_hi:[0,1,1]
	v_and_b32_e32 v75, 0xffff0000, v47
	v_lshlrev_b32_e32 v74, 16, v47
	v_pk_fma_f32 v[72:73], v[162:163], v[74:75], v[72:73] op_sel_hi:[0,1,1]
	v_and_b32_e32 v75, 0xffff0000, v51
	v_lshlrev_b32_e32 v74, 16, v51
	v_pk_fma_f32 v[72:73], v[164:165], v[74:75], v[72:73] op_sel_hi:[0,1,1]
	v_and_b32_e32 v75, 0xffff0000, v55
	v_lshlrev_b32_e32 v74, 16, v55
	v_pk_fma_f32 v[72:73], v[166:167], v[74:75], v[72:73] op_sel_hi:[0,1,1]
	v_and_b32_e32 v75, 0xffff0000, v59
	v_lshlrev_b32_e32 v74, 16, v59
	v_pk_fma_f32 v[72:73], v[168:169], v[74:75], v[72:73] op_sel_hi:[0,1,1]
	v_and_b32_e32 v75, 0xffff0000, v63
	v_lshlrev_b32_e32 v74, 16, v63
	v_pk_fma_f32 v[72:73], v[170:171], v[74:75], v[72:73] op_sel_hi:[0,1,1]
	v_cvt_pk_bf16_f32 v70, v70, v71
	v_cvt_pk_bf16_f32 v71, v72, v73
	v_and_b32_e32 v73, 0xffff0000, v36
	v_lshlrev_b32_e32 v72, 16, v36
	v_pk_fma_f32 v[72:73], v[156:157], v[72:73], 0 op_sel_hi:[0,1,0]
	v_and_b32_e32 v75, 0xffff0000, v40
	v_lshlrev_b32_e32 v74, 16, v40
	v_pk_fma_f32 v[72:73], v[158:159], v[74:75], v[72:73] op_sel_hi:[0,1,1]
	v_and_b32_e32 v75, 0xffff0000, v44
	v_lshlrev_b32_e32 v74, 16, v44
	v_pk_fma_f32 v[72:73], v[160:161], v[74:75], v[72:73] op_sel_hi:[0,1,1]
	v_and_b32_e32 v75, 0xffff0000, v48
	v_lshlrev_b32_e32 v74, 16, v48
	v_pk_fma_f32 v[72:73], v[162:163], v[74:75], v[72:73] op_sel_hi:[0,1,1]
	v_and_b32_e32 v75, 0xffff0000, v52
	v_lshlrev_b32_e32 v74, 16, v52
	v_pk_fma_f32 v[72:73], v[164:165], v[74:75], v[72:73] op_sel_hi:[0,1,1]
	v_and_b32_e32 v75, 0xffff0000, v56
	v_lshlrev_b32_e32 v74, 16, v56
	v_pk_fma_f32 v[72:73], v[166:167], v[74:75], v[72:73] op_sel_hi:[0,1,1]
	v_and_b32_e32 v75, 0xffff0000, v60
	v_lshlrev_b32_e32 v74, 16, v60
	v_pk_fma_f32 v[72:73], v[168:169], v[74:75], v[72:73] op_sel_hi:[0,1,1]
	v_and_b32_e32 v75, 0xffff0000, v64
	v_lshlrev_b32_e32 v74, 16, v64
	v_pk_fma_f32 v[72:73], v[170:171], v[74:75], v[72:73] op_sel_hi:[0,1,1]
	v_and_b32_e32 v75, 0xffff0000, v37
	v_lshlrev_b32_e32 v74, 16, v37
	v_pk_fma_f32 v[74:75], v[156:157], v[74:75], 0 op_sel_hi:[0,1,0]
	v_and_b32_e32 v77, 0xffff0000, v41
	v_lshlrev_b32_e32 v76, 16, v41
	v_pk_fma_f32 v[74:75], v[158:159], v[76:77], v[74:75] op_sel_hi:[0,1,1]
	v_and_b32_e32 v77, 0xffff0000, v45
	v_lshlrev_b32_e32 v76, 16, v45
	v_pk_fma_f32 v[74:75], v[160:161], v[76:77], v[74:75] op_sel_hi:[0,1,1]
	v_and_b32_e32 v77, 0xffff0000, v49
	v_lshlrev_b32_e32 v76, 16, v49
	v_pk_fma_f32 v[74:75], v[162:163], v[76:77], v[74:75] op_sel_hi:[0,1,1]
	v_and_b32_e32 v77, 0xffff0000, v53
	v_lshlrev_b32_e32 v76, 16, v53
	v_pk_fma_f32 v[74:75], v[164:165], v[76:77], v[74:75] op_sel_hi:[0,1,1]
	v_and_b32_e32 v77, 0xffff0000, v57
	v_lshlrev_b32_e32 v76, 16, v57
	v_pk_fma_f32 v[74:75], v[166:167], v[76:77], v[74:75] op_sel_hi:[0,1,1]
	v_and_b32_e32 v77, 0xffff0000, v61
	v_lshlrev_b32_e32 v76, 16, v61
	v_pk_fma_f32 v[74:75], v[168:169], v[76:77], v[74:75] op_sel_hi:[0,1,1]
	v_and_b32_e32 v77, 0xffff0000, v65
	v_lshlrev_b32_e32 v76, 16, v65
	v_pk_fma_f32 v[74:75], v[170:171], v[76:77], v[74:75] op_sel_hi:[0,1,1]
	v_cvt_pk_bf16_f32 v72, v72, v73
	v_cvt_pk_bf16_f32 v73, v74, v75
	v_readlane_b32 s10, v254, 53
	s_waitcnt vmcnt(0)
	s_add_i32 s9, s10, s9
	s_min_i32 s9, s8, s9
	s_cmp_ge_i32 s12, s9
	s_cbranch_scc1 .LBB0_709
	v_readfirstlane_b32 s0, v138
	s_nop 3
	s_cmp_lt_u32 s0, 16
	s_cbranch_scc1 .Lstagger_skip
	s_sleep 55
